# input row-norm: wave sum by DPP row ops + readlane instead of six bpermute round trips (on top of v59)
# baseline (speedup 1.0000x reference)
.LBB0_48:
	global_load_dwordx4 v[14:17], v[38:39], off offset:-4096
	global_load_dwordx4 v[2:5], v[38:39], off offset:-3072
	global_load_dwordx4 v[10:13], v[38:39], off offset:-2048
	global_load_dwordx4 v[6:9], v[38:39], off
	global_load_dwordx4 v[18:21], v[38:39], off offset:-1024
	global_load_dwordx4 v[26:29], v[38:39], off offset:1024
	global_load_dwordx4 v[22:25], v[38:39], off offset:3072
	global_load_dwordx4 v[30:33], v[38:39], off offset:2048
	s_waitcnt vmcnt(7)
	v_mov_b32_e32 v48, v15
	s_waitcnt vmcnt(6)
	v_mov_b32_e32 v49, v3
	v_mov_b32_e32 v52, v17
	v_mov_b32_e32 v53, v5
	v_mov_b32_e32 v46, v14
	v_mov_b32_e32 v47, v2
	v_mov_b32_e32 v50, v16
	v_mov_b32_e32 v51, v4
	s_waitcnt vmcnt(5)
	v_pk_mul_f32 v[54:55], v[12:13], v[12:13]
	v_pk_mul_f32 v[56:57], v[10:11], v[10:11]
	v_pk_mul_f32 v[48:49], v[48:49], v[48:49]
	v_pk_mul_f32 v[52:53], v[52:53], v[52:53]
	v_pk_mov_b32 v[70:71], v[56:57], v[54:55] op_sel:[1,0]
	v_mov_b32_e32 v57, v55
	v_pk_fma_f32 v[46:47], v[46:47], v[46:47], v[48:49]
	v_pk_fma_f32 v[48:49], v[50:51], v[50:51], v[52:53]
	s_waitcnt vmcnt(3)
	v_mul_f32_e32 v58, v19, v19
	v_mul_f32_e32 v60, v21, v21
	v_pk_add_f32 v[50:51], v[70:71], v[56:57]
	v_pk_add_f32 v[46:47], v[46:47], v[48:49]
	v_mul_f32_e32 v45, v6, v6
	v_mul_f32_e32 v69, v7, v7
	v_mul_f32_e32 v72, v8, v8
	v_mul_f32_e32 v73, v9, v9
	v_pk_fma_f32 v[54:55], v[18:19], v[18:19], v[58:59] op_sel_hi:[1,1,0]
	v_pk_fma_f32 v[58:59], v[20:21], v[20:21], v[60:61] op_sel_hi:[1,1,0]
	v_pk_add_f32 v[48:49], v[50:51], v[50:51] op_sel:[0,1] op_sel_hi:[1,0]
	v_pk_add_f32 v[46:47], v[46:47], v[46:47] op_sel:[0,1] op_sel_hi:[1,0]
	s_waitcnt vmcnt(2)
	v_pk_mul_f32 v[62:63], v[28:29], v[28:29]
	v_pk_mul_f32 v[64:65], v[26:27], v[26:27]
	v_mov_b32_e32 v55, v72
	v_mov_b32_e32 v59, v73
	v_mov_b32_e32 v49, v69
	v_mov_b32_e32 v47, v45
	v_pk_mov_b32 v[60:61], v[64:65], v[62:63] op_sel:[1,0]
	v_mov_b32_e32 v65, v63
	v_pk_add_f32 v[50:51], v[54:55], v[58:59]
	v_pk_add_f32 v[46:47], v[46:47], v[48:49]
	s_waitcnt vmcnt(0)
	v_mul_f32_e32 v66, v31, v31
	v_mul_f32_e32 v68, v33, v33
	v_pk_add_f32 v[52:53], v[60:61], v[64:65]
	v_pk_add_f32 v[46:47], v[46:47], v[50:51]
	v_mul_f32_e32 v74, v22, v22
	v_mul_f32_e32 v75, v23, v23
	v_mul_f32_e32 v76, v24, v24
	v_mul_f32_e32 v77, v25, v25
	v_pk_fma_f32 v[62:63], v[30:31], v[30:31], v[66:67] op_sel_hi:[1,1,0]
	v_pk_fma_f32 v[66:67], v[32:33], v[32:33], v[68:69] op_sel_hi:[1,1,0]
	v_pk_add_f32 v[52:53], v[52:53], v[52:53] op_sel:[0,1] op_sel_hi:[1,0]
	v_pk_add_f32 v[46:47], v[46:47], v[46:47] op_sel:[0,1] op_sel_hi:[1,0]
	v_mov_b32_e32 v63, v76
	v_mov_b32_e32 v67, v77
	v_mov_b32_e32 v53, v75
	v_mov_b32_e32 v47, v74
	v_pk_add_f32 v[54:55], v[62:63], v[66:67]
	v_pk_add_f32 v[46:47], v[46:47], v[52:53]
	s_nop 0
	v_pk_add_f32 v[46:47], v[46:47], v[54:55]
	s_nop 0
	v_add_f32_e32 v45, v46, v47
	s_nop 1
	v_add_f32_dpp v45, v45, v45 quad_perm:[1,0,3,2] row_mask:0xf bank_mask:0xf
	s_nop 1
	v_add_f32_dpp v45, v45, v45 quad_perm:[2,3,0,1] row_mask:0xf bank_mask:0xf
	s_nop 1
	v_add_f32_dpp v45, v45, v45 row_ror:4 row_mask:0xf bank_mask:0xf
	s_nop 1
	v_add_f32_dpp v45, v45, v45 row_ror:8 row_mask:0xf bank_mask:0xf
	s_nop 1
	v_add_f32_dpp v45, v45, v45 row_bcast:15 row_mask:0xa bank_mask:0xf
	s_nop 1
	v_add_f32_dpp v45, v45, v45 row_bcast:31 row_mask:0xc bank_mask:0xf
	s_nop 1
	v_readlane_b32 s99, v45, 63
	s_nop 3
	v_mov_b32_e32 v45, s99
	v_fmamk_f32 v46, v45, 0x3a000000, v36
	v_mul_f32_e32 v45, 0x4b800000, v46
	v_cmp_gt_f32_e32 vcc, s4, v46
	s_nop 1
	v_cndmask_b32_e32 v45, v46, v45, vcc
	v_rsq_f32_e32 v45, v45
	s_nop 0
	v_mul_f32_e32 v47, 0x45800000, v45
	v_cndmask_b32_e32 v45, v45, v47, vcc
	s_and_saveexec_b64 s[18:19], s[6:7]
	s_cbranch_execz .LBB0_47
	s_add_u32 s22, s10, s2
	v_mul_f32_e32 v46, v46, v45
	s_addc_u32 s23, s11, s3
	global_store_dword v37, v46, s[22:23]
	s_branch .LBB0_47
